# v23: v10 + layer-1 expert down-proj weight bf16 conversion moved out of phase 16 onto the workgroups idle during the WKV scan (hand-written tile loop, dst in dead weight regions; phase 18 B base patch
# baseline (speedup 1.0000x reference)
.Lx14_begin:
	s_mov_b64 exec, -1
	s_cmp_lg_u32 s33, 0x100
	s_cbranch_scc1 .LBB0_1816
	s_load_dwordx2 s[4:5], s[74:75], 0x130
	s_add_i32 s25, s2, 0xffffff80
	v_lshrrev_b32_e32 v1, 3, v0
	v_and_b32_e32 v2, 7, v0
	v_lshlrev_b32_e32 v3, 13, v1
	v_lshl_add_u32 v3, v2, 5, v3
	v_mul_u32_u24_e32 v4, 0x204, v1
	v_lshl_add_u32 v4, v2, 5, v4
	v_lshrrev_b32_e32 v5, 2, v0
	v_and_b32_e32 v6, 3, v0
	v_mul_u32_u24_e32 v7, 0x2040, v6
	v_lshl_add_u32 v7, v5, 2, v7
	v_lshlrev_b32_e32 v8, 10, v5
	v_lshl_add_u32 v8, v6, 5, v8
	s_waitcnt vmcnt(0) lgkmcnt(0)
	s_add_u32 s4, s4, 0x8000000
	s_addc_u32 s5, s5, 0
	s_add_u32 s6, s54, 0x1400000
	s_addc_u32 s7, s55, 0
.Lxcv_tile:
	s_lshr_b32 s8, s25, 7
	s_bfe_u32 s9, s25, 0x40003
	s_and_b32 s10, s25, 7
	s_lshl_b32 s11, s8, 22
	s_lshl_b32 s12, s10, 19
	s_add_i32 s11, s11, s12
	s_lshl_b32 s12, s9, 9
	s_add_i32 s11, s11, s12
	s_add_u32 s14, s4, s11
	s_addc_u32 s15, s5, 0
	global_load_dwordx4 v[10:13], v3, s[14:15]
	global_load_dwordx4 v[14:17], v3, s[14:15] offset:16
	global_load_dwordx4 v[18:21], v3, s[14:15] offset:256
	global_load_dwordx4 v[22:25], v3, s[14:15] offset:272
	s_lshl_b32 s11, s8, 21
	s_lshl_b32 s12, s9, 17
	s_add_i32 s11, s11, s12
	s_lshl_b32 s12, s10, 7
	s_add_i32 s11, s11, s12
	s_cmp_ge_u32 s8, 25
	s_cselect_b32 s12, 0x1000000, 0
	s_add_i32 s11, s11, s12
	s_add_u32 s16, s6, s11
	s_addc_u32 s17, s7, 0
	s_waitcnt vmcnt(0)
	ds_write2_b32 v4, v10, v11 offset0:0 offset1:1
	ds_write2_b32 v4, v12, v13 offset0:2 offset1:3
	ds_write2_b32 v4, v14, v15 offset0:4 offset1:5
	ds_write2_b32 v4, v16, v17 offset0:6 offset1:7
	ds_write2_b32 v4, v18, v19 offset0:64 offset1:65
	ds_write2_b32 v4, v20, v21 offset0:66 offset1:67
	ds_write2_b32 v4, v22, v23 offset0:68 offset1:69
	ds_write2_b32 v4, v24, v25 offset0:70 offset1:71
	s_waitcnt lgkmcnt(0)
	s_barrier
	ds_read_b32 v30, v7
	ds_read_b32 v31, v7 offset:516
	ds_read_b32 v32, v7 offset:1032
	ds_read_b32 v33, v7 offset:1548
	ds_read_b32 v34, v7 offset:2064
	ds_read_b32 v35, v7 offset:2580
	ds_read_b32 v36, v7 offset:3096
	ds_read_b32 v37, v7 offset:3612
	ds_read_b32 v38, v7 offset:4128
	ds_read_b32 v39, v7 offset:4644
	ds_read_b32 v40, v7 offset:5160
	ds_read_b32 v41, v7 offset:5676
	ds_read_b32 v42, v7 offset:6192
	ds_read_b32 v43, v7 offset:6708
	ds_read_b32 v44, v7 offset:7224
	ds_read_b32 v45, v7 offset:7740
	s_waitcnt lgkmcnt(0)
	v_cvt_pk_bf16_f32 v50, v30, v31
	v_cvt_pk_bf16_f32 v51, v32, v33
	v_cvt_pk_bf16_f32 v52, v34, v35
	v_cvt_pk_bf16_f32 v53, v36, v37
	v_cvt_pk_bf16_f32 v54, v38, v39
	v_cvt_pk_bf16_f32 v55, v40, v41
	v_cvt_pk_bf16_f32 v56, v42, v43
	v_cvt_pk_bf16_f32 v57, v44, v45
	global_store_dwordx4 v8, v[50:53], s[16:17]
	global_store_dwordx4 v8, v[54:57], s[16:17] offset:16
	s_barrier
	s_add_i32 s25, s25, 0x80
	s_cmp_lt_u32 s25, 0x1000
	s_cbranch_scc1 .Lxcv_tile
	s_waitcnt vmcnt(0) lgkmcnt(0)
	s_barrier
	v_cmp_eq_u32_e32 vcc, 0, v0
	s_and_saveexec_b64 s[98:99], vcc
	s_cbranch_execz .Lx14_sb_done
	buffer_wbl2 sc1
	s_waitcnt vmcnt(0)
	v_mov_b32_e32 v1, 0xc800
	v_mov_b32_e32 v2, 1
	global_atomic_add v1, v2, s[54:55]
	s_waitcnt vmcnt(0)
	s_mov_b32 s0, 0

.LBB0_2001:
	s_cmp_lg_u32 s92, s38
	s_mov_b64 s[38:39], -1
	s_cbranch_scc0 .LBB0_2017
	s_branch .LBB0_2016

.LBB0_2214:
	s_add_i32 s0, 0, 0x27c80
	v_mov_b32_e32 v1, s0
	s_waitcnt lgkmcnt(0)
	s_barrier
	ds_read_b32 v1, v1
	s_ashr_i32 s3, s2, 31
	v_mov_b64_e32 v[2:3], s[2:3]
	v_readfirstlane_b32 s40, v0
	s_waitcnt lgkmcnt(0)
	v_readfirstlane_b32 s0, v1
	s_ashr_i32 s1, s0, 31
	s_lshl_b64 s[0:1], s[0:1], 3
	v_cmp_le_i64_e32 vcc, s[0:1], v[2:3]
	s_cbranch_vccnz .LBB0_2228
	v_bfe_u32 v4, v0, 3, 25
	v_bfe_u32 v3, v0, 2, 4
	v_or_b32_e32 v4, 64, v4
	s_movk_i32 s1, 0x70
	v_lshlrev_b32_e32 v1, 4, v0
	v_and_b32_e32 v2, 32, v0
	v_and_or_b32 v147, v4, s1, v3
	s_lshr_b32 s1, s40, 6
	s_lshr_b32 s0, s40, 8
	v_bitop3_b32 v1, v1, v2, 48 bitop3:0x6c
	v_lshrrev_b32_e32 v2, 3, v0
	s_lshl_b32 s41, s1, 10
	v_and_or_b32 v146, v2, 48, v3
	s_add_u32 s8, s54, 0x29400000
	v_lshrrev_b32_e32 v3, 5, v0
	v_lshrrev_b32_e32 v6, 1, v0
	s_addc_u32 s9, s55, 0
	v_and_b32_e32 v3, 4, v3
	v_bfe_u32 v5, v0, 2, 2
	v_and_b32_e32 v6, 24, v6
	s_add_u32 s42, s54, 0x1400000
	v_or3_b32 v3, v3, v5, v6
	v_and_or_b32 v1, v0, 64, v1
	s_addc_u32 s43, s55, 0
	v_and_or_b32 v2, v2, 32, v3
	s_add_i32 s10, 0, 0x27c04
	s_movk_i32 s4, 0x60
	v_lshl_or_b32 v132, v2, 10, v1
	v_mov_b32_e32 v2, s10
	v_and_or_b32 v4, v4, s4, v3
	ds_read2_b32 v[2:3], v2 offset1:1
	s_add_i32 s10, 0, 0x27c0c
	v_lshl_or_b32 v130, v4, 10, v1
	v_mov_b32_e32 v4, s10
	s_add_i32 s10, 0, 0x27c14
	s_lshr_b32 s4, s3, 29
	v_mov_b32_e32 v7, s10
	s_add_i32 s10, 0, 0x27c1c
	s_add_i32 s4, s2, s4
	v_mov_b32_e32 v10, s10
	s_ashr_i32 s5, s4, 3
	ds_read2_b32 v[4:5], v4 offset1:1
	ds_read2_b32 v[8:9], v7 offset1:1
	ds_read2_b32 v[10:11], v10 offset1:1
	s_waitcnt lgkmcnt(3)
	v_cmp_ge_i32_e32 vcc, s5, v2
	s_add_i32 s10, 0, 0x27c24
	s_and_b32 s4, s4, 0xfffff8
	v_cndmask_b32_e64 v2, 0, 1, vcc
	v_cmp_lt_i32_e32 vcc, s5, v3
	s_sub_i32 s4, s2, s4
	s_lshl_b32 s82, s5, 8
	v_cndmask_b32_e32 v2, 2, v2, vcc
	s_waitcnt lgkmcnt(2)
	v_cmp_lt_i32_e32 vcc, s5, v4
	s_lshl_b32 s81, s4, 8
	v_or_b32_e32 v148, 0x80, v146
	v_cndmask_b32_e32 v2, 3, v2, vcc
	v_cmp_lt_i32_e32 vcc, s5, v5
	v_or_b32_e32 v149, 0x80, v147
	v_mov_b32_e32 v135, 0
	v_cndmask_b32_e32 v2, 4, v2, vcc
	s_waitcnt lgkmcnt(1)
	v_cmp_lt_i32_e32 vcc, s5, v8
	v_mov_b32_e32 v133, v135
	v_mov_b32_e32 v131, v135
	v_cndmask_b32_e32 v2, 5, v2, vcc
	v_cmp_lt_i32_e32 vcc, s5, v9
	s_mov_b32 s48, 0x10000
	v_mov_b32_e32 v137, v135
	v_cndmask_b32_e32 v2, 6, v2, vcc
	s_waitcnt lgkmcnt(0)
	v_cmp_lt_i32_e32 vcc, s5, v10
	s_nop 1
	v_cndmask_b32_e32 v2, 7, v2, vcc
	v_cmp_lt_i32_e32 vcc, s5, v11
	s_nop 1
	v_cndmask_b32_e32 v7, 8, v2, vcc
	v_mov_b32_e32 v2, s10
	ds_read2_b32 v[2:3], v2 offset1:1
	s_add_i32 s10, 0, 0x27c2c
	v_mov_b32_e32 v4, s10
	s_add_i32 s10, 0, 0x27c34
	v_mov_b32_e32 v8, s10
	s_add_i32 s10, 0, 0x27c3c
	v_mov_b32_e32 v10, s10
	ds_read2_b32 v[4:5], v4 offset1:1
	ds_read2_b32 v[8:9], v8 offset1:1
	ds_read2_b32 v[10:11], v10 offset1:1
	s_waitcnt lgkmcnt(3)
	v_cmp_lt_i32_e32 vcc, s5, v2
	s_add_i32 s10, 0, 0x27c44
	s_nop 0
	v_cndmask_b32_e32 v2, 9, v7, vcc
	v_cmp_lt_i32_e32 vcc, s5, v3
	s_nop 1
	v_cndmask_b32_e32 v2, 10, v2, vcc
	s_waitcnt lgkmcnt(2)
	v_cmp_lt_i32_e32 vcc, s5, v4
	s_nop 1
	v_cndmask_b32_e32 v2, 11, v2, vcc
	v_cmp_lt_i32_e32 vcc, s5, v5
	s_nop 1
	v_cndmask_b32_e32 v2, 12, v2, vcc
	s_waitcnt lgkmcnt(1)
	v_cmp_lt_i32_e32 vcc, s5, v8
	s_nop 1
	v_cndmask_b32_e32 v2, 13, v2, vcc
	v_cmp_lt_i32_e32 vcc, s5, v9
	s_nop 1
	v_cndmask_b32_e32 v2, 14, v2, vcc
	s_waitcnt lgkmcnt(0)
	v_cmp_lt_i32_e32 vcc, s5, v10
	s_nop 1
	v_cndmask_b32_e32 v2, 15, v2, vcc
	v_cmp_lt_i32_e32 vcc, s5, v11
	s_nop 1
	v_cndmask_b32_e32 v7, 16, v2, vcc
	v_mov_b32_e32 v2, s10
	ds_read2_b32 v[2:3], v2 offset1:1
	s_add_i32 s10, 0, 0x27c4c
	v_mov_b32_e32 v4, s10
	s_add_i32 s10, 0, 0x27c54
	v_mov_b32_e32 v8, s10
	s_add_i32 s10, 0, 0x27c5c
	v_mov_b32_e32 v10, s10
	ds_read2_b32 v[4:5], v4 offset1:1
	ds_read2_b32 v[8:9], v8 offset1:1
	ds_read2_b32 v[10:11], v10 offset1:1
	s_waitcnt lgkmcnt(3)
	v_cmp_lt_i32_e32 vcc, s5, v2
	s_add_i32 s10, 0, 0x27c64
	s_nop 0
	v_cndmask_b32_e32 v2, 17, v7, vcc
	v_cmp_lt_i32_e32 vcc, s5, v3
	s_nop 1
	v_cndmask_b32_e32 v2, 18, v2, vcc
	s_waitcnt lgkmcnt(2)
	v_cmp_lt_i32_e32 vcc, s5, v4
	s_nop 1
	v_cndmask_b32_e32 v2, 19, v2, vcc
	v_cmp_lt_i32_e32 vcc, s5, v5
	s_nop 1
	v_cndmask_b32_e32 v2, 20, v2, vcc
	s_waitcnt lgkmcnt(1)
	v_cmp_lt_i32_e32 vcc, s5, v8
	s_nop 1
	v_cndmask_b32_e32 v2, 21, v2, vcc
	v_cmp_lt_i32_e32 vcc, s5, v9
	s_nop 1
	v_cndmask_b32_e32 v2, 22, v2, vcc
	s_waitcnt lgkmcnt(0)
	v_cmp_lt_i32_e32 vcc, s5, v10
	s_nop 1
	v_cndmask_b32_e32 v2, 23, v2, vcc
	v_cmp_lt_i32_e32 vcc, s5, v11
	s_nop 1
	v_cndmask_b32_e32 v7, 24, v2, vcc
	v_mov_b32_e32 v2, s10
	ds_read2_b32 v[2:3], v2 offset1:1
	s_add_i32 s10, 0, 0x27c6c
	v_mov_b32_e32 v4, s10
	s_add_i32 s10, 0, 0x27c74
	v_mov_b32_e32 v8, s10
	s_add_i32 s10, 0, 0x27c7c
	v_mov_b32_e32 v10, s10
	ds_read2_b32 v[4:5], v4 offset1:1
	ds_read2_b32 v[8:9], v8 offset1:1
	ds_read_b32 v10, v10
	s_waitcnt lgkmcnt(3)
	v_cmp_lt_i32_e32 vcc, s5, v2
	s_nop 1
	v_cndmask_b32_e32 v2, 25, v7, vcc
	v_cmp_lt_i32_e32 vcc, s5, v3
	s_nop 1
	v_cndmask_b32_e32 v2, 26, v2, vcc
	s_waitcnt lgkmcnt(2)
	v_cmp_lt_i32_e32 vcc, s5, v4
	s_nop 1
	v_cndmask_b32_e32 v2, 27, v2, vcc
	v_cmp_lt_i32_e32 vcc, s5, v5
	s_nop 1
	v_cndmask_b32_e32 v2, 28, v2, vcc
	s_waitcnt lgkmcnt(1)
	v_cmp_lt_i32_e32 vcc, s5, v8
	s_nop 1
	v_cndmask_b32_e32 v2, 29, v2, vcc
	v_cmp_lt_i32_e32 vcc, s5, v9
	s_nop 1
	v_cndmask_b32_e32 v2, 30, v2, vcc
	s_waitcnt lgkmcnt(0)
	v_cmp_lt_i32_e32 vcc, s5, v10
	s_nop 1
	v_cndmask_b32_e32 v2, 31, v2, vcc
	s_nop 0
	v_readfirstlane_b32 s10, v2
	s_lshl_b32 s5, s10, 11
	s_add_i32 s4, s5, s81
	s_ashr_i32 s5, s4, 31
	s_lshl_b64 s[4:5], s[4:5], 10
	s_add_u32 s36, s42, s4
	s_addc_u32 s37, s43, s5
	s_cmp_ge_u32 s10, 25
	s_cselect_b32 s98, 0x1000000, 0
	s_add_u32 s36, s36, s98
	s_addc_u32 s37, s37, 0
	s_add_i32 s44, s41, 0
	v_or_b32_e32 v2, s82, v146
	s_add_i32 m0, s44, 0x10000
	v_lshl_or_b32 v134, v2, 10, v1
	v_or_b32_e32 v2, s82, v148
	global_load_lds_dwordx4 v132, s[36:37]
	s_add_i32 m0, s44, 0x12000
	v_lshl_or_b32 v138, v2, 10, v1
	v_or_b32_e32 v2, s82, v147
	global_load_lds_dwordx4 v130, s[36:37]
	s_mov_b32 m0, s44
	s_add_i32 s45, s44, 0x2000
	v_lshl_or_b32 v136, v2, 10, v1
	global_load_lds_dwordx4 v134, s[8:9]
	s_mov_b32 m0, s45
	s_add_u32 s4, s36, 0x20000
	global_load_lds_dwordx4 v136, s[8:9]
	s_addc_u32 s5, s37, 0
	s_add_i32 m0, s44, 0x14000
	s_add_i32 s46, s44, 0x4000
	global_load_lds_dwordx4 v132, s[4:5]
	s_add_i32 m0, s44, 0x16000
	v_or_b32_e32 v2, s82, v149
	global_load_lds_dwordx4 v130, s[4:5]
	s_mov_b32 m0, s46
	s_add_i32 s47, s44, 0x6000
	v_lshl_or_b32 v140, v2, 10, v1
	global_load_lds_dwordx4 v138, s[8:9]
	s_mov_b32 m0, s47
	v_lshl_add_u64 v[4:5], s[36:37], 0, v[132:133]
	global_load_lds_dwordx4 v140, s[8:9]
	v_lshl_add_u64 v[2:3], s[36:37], 0, v[130:131]
	s_cmp_lg_u32 s0, 1
	s_mov_b64 s[10:11], 0x20000
	s_cbranch_scc1 .LBB0_2217
	s_barrier

.LBB0_2222:
	s_ashr_i32 s31, s30, 31
	s_lshl_b64 s[34:35], s[30:31], 10
	s_add_u32 s34, s42, s34
	s_addc_u32 s35, s43, s35
	s_lshr_b32 s98, s30, 11
	s_cmp_ge_u32 s98, 25
	s_cselect_b32 s98, 0x1000000, 0
	s_add_u32 s34, s34, s98
	s_addc_u32 s35, s35, 0
	s_and_b64 s[4:5], s[4:5], exec
	s_cselect_b32 s31, s35, s37
	s_cselect_b32 s85, s34, s36
	v_mov_b32_e32 v139, v135
	v_mov_b32_e32 v141, v135
	s_add_u32 s86, s36, 0x100
	v_mov_b32_e32 v2, 0
	v_lshl_add_u64 v[142:143], s[16:17], 0, v[140:141]
	v_lshl_add_u64 v[144:145], s[16:17], 0, v[138:139]
	s_addc_u32 s87, s37, 0
	s_mov_b32 s88, -2
	s_mov_b64 s[4:5], 0
	v_mov_b32_e32 v3, v2
	v_mov_b32_e32 v4, v2
	v_mov_b32_e32 v5, v2
	v_mov_b32_e32 v6, v2
	v_mov_b32_e32 v7, v2
	v_mov_b32_e32 v8, v2
	v_mov_b32_e32 v9, v2
	v_mov_b32_e32 v10, v2
	v_mov_b32_e32 v11, v2
	v_mov_b32_e32 v12, v2
	v_mov_b32_e32 v13, v2
	v_mov_b32_e32 v14, v2
	v_mov_b32_e32 v15, v2
	v_mov_b32_e32 v16, v2
	v_mov_b32_e32 v17, v2
	v_mov_b32_e32 v22, v2
	v_mov_b32_e32 v23, v2
	v_mov_b32_e32 v24, v2
	v_mov_b32_e32 v25, v2
	v_mov_b32_e32 v30, v2
	v_mov_b32_e32 v31, v2
	v_mov_b32_e32 v32, v2
	v_mov_b32_e32 v33, v2
	v_mov_b32_e32 v42, v2
	v_mov_b32_e32 v43, v2
	v_mov_b32_e32 v44, v2
	v_mov_b32_e32 v45, v2
	v_mov_b32_e32 v46, v2
	v_mov_b32_e32 v47, v2
	v_mov_b32_e32 v48, v2
	v_mov_b32_e32 v49, v2
	v_mov_b32_e32 v74, v2
	v_mov_b32_e32 v75, v2
	v_mov_b32_e32 v76, v2
	v_mov_b32_e32 v77, v2
	v_mov_b32_e32 v82, v2
	v_mov_b32_e32 v83, v2
	v_mov_b32_e32 v84, v2
	v_mov_b32_e32 v85, v2
	v_mov_b32_e32 v90, v2
	v_mov_b32_e32 v91, v2
	v_mov_b32_e32 v92, v2
	v_mov_b32_e32 v93, v2
	v_mov_b32_e32 v94, v2
	v_mov_b32_e32 v95, v2
	v_mov_b32_e32 v96, v2
	v_mov_b32_e32 v97, v2
	v_mov_b32_e32 v18, v2
	v_mov_b32_e32 v19, v2
	v_mov_b32_e32 v20, v2
	v_mov_b32_e32 v21, v2
	v_mov_b32_e32 v26, v2
	v_mov_b32_e32 v27, v2
	v_mov_b32_e32 v28, v2
	v_mov_b32_e32 v29, v2
	v_mov_b32_e32 v34, v2
	v_mov_b32_e32 v35, v2
	v_mov_b32_e32 v36, v2
	v_mov_b32_e32 v37, v2
	v_mov_b32_e32 v38, v2
	v_mov_b32_e32 v39, v2
	v_mov_b32_e32 v40, v2
	v_mov_b32_e32 v41, v2
	v_mov_b32_e32 v62, v2
	v_mov_b32_e32 v63, v2
	v_mov_b32_e32 v64, v2
	v_mov_b32_e32 v65, v2
	v_mov_b32_e32 v70, v2
	v_mov_b32_e32 v71, v2
	v_mov_b32_e32 v72, v2
	v_mov_b32_e32 v73, v2
	v_mov_b32_e32 v78, v2
	v_mov_b32_e32 v79, v2
	v_mov_b32_e32 v80, v2
	v_mov_b32_e32 v81, v2
	v_mov_b32_e32 v86, v2
	v_mov_b32_e32 v87, v2
	v_mov_b32_e32 v88, v2
	v_mov_b32_e32 v89, v2
	v_mov_b32_e32 v98, v2
	v_mov_b32_e32 v99, v2
	v_mov_b32_e32 v100, v2
	v_mov_b32_e32 v101, v2
	v_mov_b32_e32 v102, v2
	v_mov_b32_e32 v103, v2
	v_mov_b32_e32 v104, v2
	v_mov_b32_e32 v105, v2
	v_mov_b32_e32 v106, v2
	v_mov_b32_e32 v107, v2
	v_mov_b32_e32 v108, v2
	v_mov_b32_e32 v109, v2
	v_mov_b32_e32 v110, v2
	v_mov_b32_e32 v111, v2
	v_mov_b32_e32 v112, v2
	v_mov_b32_e32 v113, v2
	v_mov_b32_e32 v114, v2
	v_mov_b32_e32 v115, v2
	v_mov_b32_e32 v116, v2
	v_mov_b32_e32 v117, v2
	v_mov_b32_e32 v118, v2
	v_mov_b32_e32 v119, v2
	v_mov_b32_e32 v120, v2
	v_mov_b32_e32 v121, v2
	v_mov_b32_e32 v122, v2
	v_mov_b32_e32 v123, v2
	v_mov_b32_e32 v124, v2
	v_mov_b32_e32 v125, v2
	v_mov_b32_e32 v126, v2
	v_mov_b32_e32 v127, v2
	v_mov_b32_e32 v128, v2
	v_mov_b32_e32 v129, v2
	v_mov_b32_e32 v54, v2
	v_mov_b32_e32 v55, v2
	v_mov_b32_e32 v56, v2
	v_mov_b32_e32 v57, v2
	v_mov_b32_e32 v66, v2
	v_mov_b32_e32 v67, v2
	v_mov_b32_e32 v68, v2
	v_mov_b32_e32 v69, v2
	v_mov_b32_e32 v50, v2
	v_mov_b32_e32 v51, v2
	v_mov_b32_e32 v52, v2
	v_mov_b32_e32 v53, v2
	v_mov_b32_e32 v58, v2
	v_mov_b32_e32 v59, v2
	v_mov_b32_e32 v60, v2
	v_mov_b32_e32 v61, v2
